# grid-barrier census computed by thread 0 during the phase-0 wait instead of on the first barrier's arrival path
# baseline (speedup 1.0000x reference)
.LBB0_63:
	s_or_b64 exec, exec, s[8:9]
	s_barrier
	s_waitcnt lgkmcnt(0)
	s_mov_b32 s0, s98
	v_mbcnt_lo_u32_b32 v0, -1, 0
	v_mbcnt_hi_u32_b32 v0, -1, v0
	s_nop 1
	v_lshl_add_u32 v0, s0, 6, v0
	s_nop 0
	v_cmp_eq_u32_e32 vcc, 0, v0
	s_and_saveexec_b64 s[0:1], vcc
	s_cbranch_execz .LBB0_72
	s_mov_b32 s21, s3
	s_mov_b64 s[22:23], s[0:1]

.Lce_b106:
	v_readlane_b32 s0, v249, 34
	s_cmp_eq_u32 s0, 0
	s_cselect_b64 vcc, -1, 0
	s_cmp_eq_u32 s0, 1
	v_cndmask_b32_e32 v16, 0, v15, vcc
	s_cselect_b64 vcc, -1, 0
	s_cmp_eq_u32 s0, 2
	v_cndmask_b32_e32 v16, v16, v0, vcc
	s_cselect_b64 vcc, -1, 0
	s_cmp_eq_u32 s0, 3
	v_cndmask_b32_e32 v16, v16, v1, vcc
	s_cselect_b64 vcc, -1, 0
	s_cmp_eq_u32 s0, 4
	v_cndmask_b32_e32 v16, v16, v2, vcc
	s_cselect_b64 vcc, -1, 0
	s_cmp_eq_u32 s0, 5
	v_cndmask_b32_e32 v16, v16, v3, vcc
	s_cselect_b64 vcc, -1, 0
	s_cmp_eq_u32 s0, 6
	v_cndmask_b32_e32 v16, v16, v4, vcc
	s_cselect_b64 vcc, -1, 0
	s_cmp_eq_u32 s0, 7
	v_cndmask_b32_e32 v16, v16, v5, vcc
	s_cselect_b64 vcc, -1, 0
	s_cmp_eq_u32 s0, 8
	v_cndmask_b32_e32 v16, v16, v6, vcc
	s_cselect_b64 vcc, -1, 0
	s_cmp_eq_u32 s0, 9
	v_cndmask_b32_e32 v16, v16, v7, vcc
	s_cselect_b64 vcc, -1, 0
	s_cmp_eq_u32 s0, 10
	v_cndmask_b32_e32 v16, v16, v8, vcc
	s_cselect_b64 vcc, -1, 0
	s_cmp_eq_u32 s0, 11
	v_cndmask_b32_e32 v16, v16, v9, vcc
	s_cselect_b64 vcc, -1, 0
	s_cmp_eq_u32 s0, 12
	v_cndmask_b32_e32 v16, v16, v10, vcc
	s_cselect_b64 vcc, -1, 0
	s_cmp_eq_u32 s0, 13
	v_cndmask_b32_e32 v16, v16, v11, vcc
	s_cselect_b64 vcc, -1, 0
	s_cmp_eq_u32 s0, 14
	v_cndmask_b32_e32 v16, v16, v12, vcc
	s_cselect_b64 vcc, -1, 0
	s_cmp_eq_u32 s0, 15
	v_cndmask_b32_e32 v16, v16, v13, vcc
	s_cselect_b64 vcc, -1, 0
	v_cndmask_b32_e32 v16, v16, v14, vcc
	v_cmp_ne_u32_e32 vcc, 0, v15
	s_add_i32 s0, 0, 0x24800
	s_nop 0
	v_cndmask_b32_e64 v15, 0, 1, vcc
	v_cmp_ne_u32_e32 vcc, 0, v0
	s_nop 1
	v_addc_co_u32_e32 v0, vcc, 0, v15, vcc
	v_cmp_ne_u32_e32 vcc, 0, v1
	s_nop 1
	v_cndmask_b32_e64 v1, 0, 1, vcc
	v_cmp_ne_u32_e32 vcc, 0, v2
	v_mov_b32_e32 v2, s0
	s_add_i32 s0, 0, 0x24804
	v_addc_co_u32_e32 v0, vcc, v0, v1, vcc
	v_cmp_ne_u32_e32 vcc, 0, v3
	s_nop 1
	v_cndmask_b32_e64 v1, 0, 1, vcc
	v_cmp_ne_u32_e32 vcc, 0, v4
	s_nop 1
	v_addc_co_u32_e32 v0, vcc, v0, v1, vcc
	v_cmp_ne_u32_e32 vcc, 0, v5
	s_nop 1
	v_cndmask_b32_e64 v1, 0, 1, vcc
	v_cmp_ne_u32_e32 vcc, 0, v6
	s_nop 1
	v_addc_co_u32_e32 v0, vcc, v0, v1, vcc
	v_cmp_ne_u32_e32 vcc, 0, v7
	s_nop 1
	v_cndmask_b32_e64 v1, 0, 1, vcc
	v_cmp_ne_u32_e32 vcc, 0, v8
	s_nop 1
	v_addc_co_u32_e32 v0, vcc, v0, v1, vcc
	v_cmp_ne_u32_e32 vcc, 0, v9
	s_nop 1
	v_cndmask_b32_e64 v1, 0, 1, vcc
	v_cmp_ne_u32_e32 vcc, 0, v10
	s_nop 1
	v_addc_co_u32_e32 v0, vcc, v0, v1, vcc
	v_cmp_ne_u32_e32 vcc, 0, v11
	s_nop 1
	v_cndmask_b32_e64 v1, 0, 1, vcc
	v_cmp_ne_u32_e32 vcc, 0, v12
	s_nop 1
	v_addc_co_u32_e32 v0, vcc, v0, v1, vcc
	v_cmp_ne_u32_e32 vcc, 0, v13
	s_nop 1
	v_cndmask_b32_e64 v1, 0, 1, vcc
	v_cmp_ne_u32_e32 vcc, 0, v14
	s_nop 1
	v_addc_co_u32_e32 v0, vcc, v0, v1, vcc
	v_max_u32_e32 v1, 1, v16
	v_max_u32_e32 v0, 1, v0
	ds_write_b32 v2, v1
	v_mov_b32_e32 v2, s0
	ds_write_b32 v2, v0
	s_mov_b32 s3, s21
	s_mov_b64 s[0:1], s[22:23]
	s_waitcnt lgkmcnt(0)
	s_add_u32 s6, s78, 0x8200
	s_addc_u32 s7, s79, 0
	s_mov_b32 s5, 0x400001
	v_mov_b32_e32 v0, 0
	s_movk_i32 s10, 0xbf
	s_movk_i32 s11, 0xc0
	s_branch .LBB0_66

.LBB0_77:
	v_add_u32_e32 v93, s3, v92
	v_add_u32_e32 v90, s21, v92
	v_add_u32_e32 v88, s22, v92
	s_add_u32 s18, s78, 0x8500000
	s_addc_u32 s19, s79, 0
	s_add_u32 s4, s96, 0x1000
	s_addc_u32 s5, s97, 0
	v_lshl_add_u32 v94, v92, 12, v64
	global_load_dwordx4 v[0:3], v94, s[48:49] nt
	global_load_dwordx4 v[4:7], v94, s[48:49] offset:1024 nt
	global_load_dwordx4 v[8:11], v94, s[48:49] offset:2048 nt
	global_load_dwordx4 v[12:15], v94, s[48:49] offset:3072 nt
	v_cmp_gt_i32_e32 vcc, s20, v93
	s_and_saveexec_b64 s[0:1], vcc
	v_lshl_add_u32 v95, v93, 12, v64
	global_load_dwordx4 v[16:19], v95, s[48:49] nt
	global_load_dwordx4 v[20:23], v95, s[48:49] offset:1024 nt
	global_load_dwordx4 v[24:27], v95, s[48:49] offset:2048 nt
	global_load_dwordx4 v[28:31], v95, s[48:49] offset:3072 nt
	s_or_b64 exec, exec, s[0:1]
	v_cmp_gt_i32_e32 vcc, s20, v90
	s_and_saveexec_b64 s[0:1], vcc
	v_lshl_add_u32 v96, v90, 12, v64
	global_load_dwordx4 v[32:35], v96, s[48:49] nt
	global_load_dwordx4 v[36:39], v96, s[48:49] offset:1024 nt
	global_load_dwordx4 v[40:43], v96, s[48:49] offset:2048 nt
	global_load_dwordx4 v[44:47], v96, s[48:49] offset:3072 nt
	s_or_b64 exec, exec, s[0:1]
	v_cmp_gt_i32_e32 vcc, s20, v88
	s_and_saveexec_b64 s[0:1], vcc
	v_lshl_add_u32 v97, v88, 12, v64
	global_load_dwordx4 v[48:51], v97, s[48:49] nt
	global_load_dwordx4 v[52:55], v97, s[48:49] offset:1024 nt
	global_load_dwordx4 v[56:59], v97, s[48:49] offset:2048 nt
	global_load_dwordx4 v[60:63], v97, s[48:49] offset:3072 nt
	s_or_b64 exec, exec, s[0:1]
	v_ashrrev_i32_e32 v106, 13, v92
	v_mul_i32_i24_e32 v106, 0x6000, v106
	v_add_u32_e32 v98, v106, v64
	global_load_dwordx4 v[112:115], v98, s[96:97]
	global_load_dwordx4 v[120:123], v98, s[96:97] offset:1024
	global_load_dwordx4 v[128:131], v98, s[96:97] offset:2048
	global_load_dwordx4 v[136:139], v98, s[96:97] offset:3072
	global_load_dwordx4 v[116:119], v98, s[4:5]
	global_load_dwordx4 v[124:127], v98, s[4:5] offset:1024
	global_load_dwordx4 v[132:135], v98, s[4:5] offset:2048
	global_load_dwordx4 v[140:143], v98, s[4:5] offset:3072
	v_lshl_add_u32 v102, v92, 11, v70
	v_cmp_gt_i32_e32 vcc, s20, v93
	s_and_saveexec_b64 s[0:1], vcc
	v_ashrrev_i32_e32 v106, 13, v93
	v_mul_i32_i24_e32 v106, 0x6000, v106
	v_add_u32_e32 v99, v106, v64
	global_load_dwordx4 v[144:147], v99, s[96:97]
	global_load_dwordx4 v[152:155], v99, s[96:97] offset:1024
	global_load_dwordx4 v[160:163], v99, s[96:97] offset:2048
	global_load_dwordx4 v[168:171], v99, s[96:97] offset:3072
	global_load_dwordx4 v[148:151], v99, s[4:5]
	global_load_dwordx4 v[156:159], v99, s[4:5] offset:1024
	global_load_dwordx4 v[164:167], v99, s[4:5] offset:2048
	global_load_dwordx4 v[172:175], v99, s[4:5] offset:3072
	v_lshl_add_u32 v103, v93, 11, v70
	s_or_b64 exec, exec, s[0:1]
	v_cmp_gt_i32_e32 vcc, s20, v90
	s_and_saveexec_b64 s[0:1], vcc
	v_ashrrev_i32_e32 v106, 13, v90
	v_mul_i32_i24_e32 v106, 0x6000, v106
	v_add_u32_e32 v100, v106, v64
	global_load_dwordx4 v[176:179], v100, s[96:97]
	global_load_dwordx4 v[184:187], v100, s[96:97] offset:1024
	global_load_dwordx4 v[192:195], v100, s[96:97] offset:2048
	global_load_dwordx4 v[200:203], v100, s[96:97] offset:3072
	global_load_dwordx4 v[180:183], v100, s[4:5]
	global_load_dwordx4 v[188:191], v100, s[4:5] offset:1024
	global_load_dwordx4 v[196:199], v100, s[4:5] offset:2048
	global_load_dwordx4 v[204:207], v100, s[4:5] offset:3072
	v_lshl_add_u32 v104, v90, 11, v70
	s_or_b64 exec, exec, s[0:1]
	v_cmp_gt_i32_e32 vcc, s20, v88
	s_and_saveexec_b64 s[0:1], vcc
	v_ashrrev_i32_e32 v106, 13, v88
	v_mul_i32_i24_e32 v106, 0x6000, v106
	v_add_u32_e32 v101, v106, v64
	global_load_dwordx4 v[208:211], v101, s[96:97]
	global_load_dwordx4 v[216:219], v101, s[96:97] offset:1024
	global_load_dwordx4 v[224:227], v101, s[96:97] offset:2048
	global_load_dwordx4 v[232:235], v101, s[96:97] offset:3072
	global_load_dwordx4 v[212:215], v101, s[4:5]
	global_load_dwordx4 v[220:223], v101, s[4:5] offset:1024
	global_load_dwordx4 v[228:231], v101, s[4:5] offset:2048
	global_load_dwordx4 v[236:239], v101, s[4:5] offset:3072
	v_lshl_add_u32 v105, v88, 11, v70
	s_or_b64 exec, exec, s[0:1]
	s_waitcnt vmcnt(0)
	v_pk_add_f32 v[118:119], v[118:119], 1.0 op_sel_hi:[1,0]
	v_pk_add_f32 v[116:117], v[116:117], 1.0 op_sel_hi:[1,0]
	v_pk_add_f32 v[126:127], v[126:127], 1.0 op_sel_hi:[1,0]
	v_pk_add_f32 v[124:125], v[124:125], 1.0 op_sel_hi:[1,0]
	v_pk_add_f32 v[134:135], v[134:135], 1.0 op_sel_hi:[1,0]
	v_pk_add_f32 v[132:133], v[132:133], 1.0 op_sel_hi:[1,0]
	v_pk_add_f32 v[142:143], v[142:143], 1.0 op_sel_hi:[1,0]
	v_pk_add_f32 v[140:141], v[140:141], 1.0 op_sel_hi:[1,0]
	v_pk_fma_f32 v[2:3], v[2:3], v[118:119], v[114:115]
	v_pk_fma_f32 v[0:1], v[0:1], v[116:117], v[112:113]
	v_pk_fma_f32 v[6:7], v[6:7], v[126:127], v[122:123]
	v_pk_fma_f32 v[4:5], v[4:5], v[124:125], v[120:121]
	v_pk_fma_f32 v[10:11], v[10:11], v[134:135], v[130:131]
	v_pk_fma_f32 v[8:9], v[8:9], v[132:133], v[128:129]
	v_pk_fma_f32 v[14:15], v[14:15], v[142:143], v[138:139]
	v_pk_fma_f32 v[12:13], v[12:13], v[140:141], v[136:137]
	v_cvt_pk_bf16_f32 v0, v0, v1
	v_cvt_pk_bf16_f32 v1, v2, v3
	v_cvt_pk_bf16_f32 v4, v4, v5
	v_cvt_pk_bf16_f32 v5, v6, v7
	v_cvt_pk_bf16_f32 v8, v8, v9
	v_cvt_pk_bf16_f32 v9, v10, v11
	v_cvt_pk_bf16_f32 v12, v12, v13
	v_cvt_pk_bf16_f32 v13, v14, v15
	global_store_dwordx2 v102, v[0:1], s[18:19]
	global_store_dwordx2 v102, v[4:5], s[18:19] offset:512
	global_store_dwordx2 v102, v[8:9], s[18:19] offset:1024
	global_store_dwordx2 v102, v[12:13], s[18:19] offset:1536
	v_cmp_gt_i32_e32 vcc, s20, v93
	s_and_saveexec_b64 s[0:1], vcc
	v_pk_add_f32 v[150:151], v[150:151], 1.0 op_sel_hi:[1,0]
	v_pk_add_f32 v[148:149], v[148:149], 1.0 op_sel_hi:[1,0]
	v_pk_add_f32 v[158:159], v[158:159], 1.0 op_sel_hi:[1,0]
	v_pk_add_f32 v[156:157], v[156:157], 1.0 op_sel_hi:[1,0]
	v_pk_add_f32 v[166:167], v[166:167], 1.0 op_sel_hi:[1,0]
	v_pk_add_f32 v[164:165], v[164:165], 1.0 op_sel_hi:[1,0]
	v_pk_add_f32 v[174:175], v[174:175], 1.0 op_sel_hi:[1,0]
	v_pk_add_f32 v[172:173], v[172:173], 1.0 op_sel_hi:[1,0]
	v_pk_fma_f32 v[18:19], v[18:19], v[150:151], v[146:147]
	v_pk_fma_f32 v[16:17], v[16:17], v[148:149], v[144:145]
	v_pk_fma_f32 v[22:23], v[22:23], v[158:159], v[154:155]
	v_pk_fma_f32 v[20:21], v[20:21], v[156:157], v[152:153]
	v_pk_fma_f32 v[26:27], v[26:27], v[166:167], v[162:163]
	v_pk_fma_f32 v[24:25], v[24:25], v[164:165], v[160:161]
	v_pk_fma_f32 v[30:31], v[30:31], v[174:175], v[170:171]
	v_pk_fma_f32 v[28:29], v[28:29], v[172:173], v[168:169]
	v_cvt_pk_bf16_f32 v16, v16, v17
	v_cvt_pk_bf16_f32 v17, v18, v19
	v_cvt_pk_bf16_f32 v20, v20, v21
	v_cvt_pk_bf16_f32 v21, v22, v23
	v_cvt_pk_bf16_f32 v24, v24, v25
	v_cvt_pk_bf16_f32 v25, v26, v27
	v_cvt_pk_bf16_f32 v28, v28, v29
	v_cvt_pk_bf16_f32 v29, v30, v31
	global_store_dwordx2 v103, v[16:17], s[18:19]
	global_store_dwordx2 v103, v[20:21], s[18:19] offset:512
	global_store_dwordx2 v103, v[24:25], s[18:19] offset:1024
	global_store_dwordx2 v103, v[28:29], s[18:19] offset:1536
	s_or_b64 exec, exec, s[0:1]
	v_cmp_gt_i32_e32 vcc, s20, v90
	s_and_saveexec_b64 s[0:1], vcc
	v_pk_add_f32 v[182:183], v[182:183], 1.0 op_sel_hi:[1,0]
	v_pk_add_f32 v[180:181], v[180:181], 1.0 op_sel_hi:[1,0]
	v_pk_add_f32 v[190:191], v[190:191], 1.0 op_sel_hi:[1,0]
	v_pk_add_f32 v[188:189], v[188:189], 1.0 op_sel_hi:[1,0]
	v_pk_add_f32 v[198:199], v[198:199], 1.0 op_sel_hi:[1,0]
	v_pk_add_f32 v[196:197], v[196:197], 1.0 op_sel_hi:[1,0]
	v_pk_add_f32 v[206:207], v[206:207], 1.0 op_sel_hi:[1,0]
	v_pk_add_f32 v[204:205], v[204:205], 1.0 op_sel_hi:[1,0]
	v_pk_fma_f32 v[34:35], v[34:35], v[182:183], v[178:179]
	v_pk_fma_f32 v[32:33], v[32:33], v[180:181], v[176:177]
	v_pk_fma_f32 v[38:39], v[38:39], v[190:191], v[186:187]
	v_pk_fma_f32 v[36:37], v[36:37], v[188:189], v[184:185]
	v_pk_fma_f32 v[42:43], v[42:43], v[198:199], v[194:195]
	v_pk_fma_f32 v[40:41], v[40:41], v[196:197], v[192:193]
	v_pk_fma_f32 v[46:47], v[46:47], v[206:207], v[202:203]
	v_pk_fma_f32 v[44:45], v[44:45], v[204:205], v[200:201]
	v_cvt_pk_bf16_f32 v32, v32, v33
	v_cvt_pk_bf16_f32 v33, v34, v35
	v_cvt_pk_bf16_f32 v36, v36, v37
	v_cvt_pk_bf16_f32 v37, v38, v39
	v_cvt_pk_bf16_f32 v40, v40, v41
	v_cvt_pk_bf16_f32 v41, v42, v43
	v_cvt_pk_bf16_f32 v44, v44, v45
	v_cvt_pk_bf16_f32 v45, v46, v47
	global_store_dwordx2 v104, v[32:33], s[18:19]
	global_store_dwordx2 v104, v[36:37], s[18:19] offset:512
	global_store_dwordx2 v104, v[40:41], s[18:19] offset:1024
	global_store_dwordx2 v104, v[44:45], s[18:19] offset:1536
	s_or_b64 exec, exec, s[0:1]
	v_cmp_gt_i32_e32 vcc, s20, v88
	s_and_saveexec_b64 s[0:1], vcc
	v_pk_add_f32 v[214:215], v[214:215], 1.0 op_sel_hi:[1,0]
	v_pk_add_f32 v[212:213], v[212:213], 1.0 op_sel_hi:[1,0]
	v_pk_add_f32 v[222:223], v[222:223], 1.0 op_sel_hi:[1,0]
	v_pk_add_f32 v[220:221], v[220:221], 1.0 op_sel_hi:[1,0]
	v_pk_add_f32 v[230:231], v[230:231], 1.0 op_sel_hi:[1,0]
	v_pk_add_f32 v[228:229], v[228:229], 1.0 op_sel_hi:[1,0]
	v_pk_add_f32 v[238:239], v[238:239], 1.0 op_sel_hi:[1,0]
	v_pk_add_f32 v[236:237], v[236:237], 1.0 op_sel_hi:[1,0]
	v_pk_fma_f32 v[50:51], v[50:51], v[214:215], v[210:211]
	v_pk_fma_f32 v[48:49], v[48:49], v[212:213], v[208:209]
	v_pk_fma_f32 v[54:55], v[54:55], v[222:223], v[218:219]
	v_pk_fma_f32 v[52:53], v[52:53], v[220:221], v[216:217]
	v_pk_fma_f32 v[58:59], v[58:59], v[230:231], v[226:227]
	v_pk_fma_f32 v[56:57], v[56:57], v[228:229], v[224:225]
	v_pk_fma_f32 v[62:63], v[62:63], v[238:239], v[234:235]
	v_pk_fma_f32 v[60:61], v[60:61], v[236:237], v[232:233]
	v_cvt_pk_bf16_f32 v48, v48, v49
	v_cvt_pk_bf16_f32 v49, v50, v51
	v_cvt_pk_bf16_f32 v52, v52, v53
	v_cvt_pk_bf16_f32 v53, v54, v55
	v_cvt_pk_bf16_f32 v56, v56, v57
	v_cvt_pk_bf16_f32 v57, v58, v59
	v_cvt_pk_bf16_f32 v60, v60, v61
	v_cvt_pk_bf16_f32 v61, v62, v63
	global_store_dwordx2 v105, v[48:49], s[18:19]
	global_store_dwordx2 v105, v[52:53], s[18:19] offset:512
	global_store_dwordx2 v105, v[56:57], s[18:19] offset:1024
	global_store_dwordx2 v105, v[60:61], s[18:19] offset:1536
	s_or_b64 exec, exec, s[0:1]
	s_mov_b64 s[0:1], 0
	s_branch .LBB0_76
